# baseline (speedup 1.0000x reference)
.LBB1_55:
	s_or_b64 exec, exec, s[2:3]
	v_and_b32_e32 v110, 63, v175
	v_lshrrev_b32_e32 v111, 6, v175
	v_lshlrev_b32_e32 v111, 4, v111
	s_movk_i32 s10, 0x556
	v_mov_b32_e32 v119, v110
	v_mul_u32_u24_e32 v112, s10, v119
	v_lshrrev_b32_e32 v112, 16, v112
	v_mul_u32_u24_e32 v113, 48, v112
	v_sub_u32_e32 v113, v119, v113
	v_add_u32_e32 v114, v111, v112
	v_mul_u32_u24_e32 v156, 0x300, v114
	v_lshl_add_u32 v156, v113, 4, v156
	v_xor_b32_e32 v159, 64, v156
	v_add_u32_e32 v115, v174, v114
	v_mul_u32_u24_e32 v115, 0x300, v115
	v_add_u32_e32 v115, v115, v118
	v_lshl_add_u32 v115, v113, 2, v115
	v_lshlrev_b32_e32 v162, 2, v115
	v_lshlrev_b32_e32 v165, 1, v115
	v_lshl_add_u32 v116, v113, 2, v118
	v_lshlrev_b32_e32 v116, 2, v116
	global_load_dwordx4 v[144:147], v116, s[50:51]
	v_add_u32_e32 v119, 64, v110
	v_mul_u32_u24_e32 v112, s10, v119
	v_lshrrev_b32_e32 v112, 16, v112
	v_mul_u32_u24_e32 v113, 48, v112
	v_sub_u32_e32 v113, v119, v113
	v_add_u32_e32 v114, v111, v112
	v_mul_u32_u24_e32 v157, 0x300, v114
	v_lshl_add_u32 v157, v113, 4, v157
	v_xor_b32_e32 v160, 64, v157
	v_add_u32_e32 v115, v174, v114
	v_mul_u32_u24_e32 v115, 0x300, v115
	v_add_u32_e32 v115, v115, v118
	v_lshl_add_u32 v115, v113, 2, v115
	v_lshlrev_b32_e32 v163, 2, v115
	v_lshlrev_b32_e32 v166, 1, v115
	v_lshl_add_u32 v116, v113, 2, v118
	v_lshlrev_b32_e32 v116, 2, v116
	global_load_dwordx4 v[148:151], v116, s[50:51]
	v_add_u32_e32 v119, 128, v110
	v_mul_u32_u24_e32 v112, s10, v119
	v_lshrrev_b32_e32 v112, 16, v112
	v_mul_u32_u24_e32 v113, 48, v112
	v_sub_u32_e32 v113, v119, v113
	v_add_u32_e32 v114, v111, v112
	v_mul_u32_u24_e32 v158, 0x300, v114
	v_lshl_add_u32 v158, v113, 4, v158
	v_xor_b32_e32 v161, 64, v158
	v_add_u32_e32 v115, v174, v114
	v_mul_u32_u24_e32 v115, 0x300, v115
	v_add_u32_e32 v115, v115, v118
	v_lshl_add_u32 v115, v113, 2, v115
	v_lshlrev_b32_e32 v164, 2, v115
	v_lshlrev_b32_e32 v167, 1, v115
	v_lshl_add_u32 v116, v113, 2, v118
	v_lshlrev_b32_e32 v116, 2, v116
	global_load_dwordx4 v[152:155], v116, s[50:51]
	global_load_dwordx2 v[120:121], v165, s[38:39] nt
	global_load_dwordx2 v[122:123], v166, s[38:39] nt
	global_load_dwordx2 v[124:125], v167, s[38:39] nt
	v_add_u32_e32 v117, 0x1800, v165
	global_load_dwordx2 v[126:127], v117, s[38:39] nt
	v_add_u32_e32 v117, 0x1800, v166
	global_load_dwordx2 v[128:129], v117, s[38:39] nt
	v_add_u32_e32 v117, 0x1800, v167
	global_load_dwordx2 v[130:131], v117, s[38:39] nt
	v_add_u32_e32 v117, 0x3000, v165
	global_load_dwordx2 v[132:133], v117, s[38:39] nt
	v_add_u32_e32 v117, 0x3000, v166
	global_load_dwordx2 v[134:135], v117, s[38:39] nt
	v_add_u32_e32 v117, 0x3000, v167
	global_load_dwordx2 v[136:137], v117, s[38:39] nt
	v_add_u32_e32 v117, 0x4800, v165
	global_load_dwordx2 v[138:139], v117, s[38:39] nt
	v_add_u32_e32 v117, 0x4800, v166
	global_load_dwordx2 v[140:141], v117, s[38:39] nt
	v_add_u32_e32 v117, 0x4800, v167
	global_load_dwordx2 v[142:143], v117, s[38:39] nt
	v_add_u32_e32 v117, 0x30000, v165
	global_load_dwordx2 v[232:233], v117, s[38:39] nt
	v_add_u32_e32 v117, 0x30000, v166
	global_load_dwordx2 v[234:235], v117, s[38:39] nt
	v_add_u32_e32 v117, 0x30000, v167
	global_load_dwordx2 v[236:237], v117, s[38:39] nt
	v_add_u32_e32 v117, 0x31800, v165
	global_load_dwordx2 v[238:239], v117, s[38:39] nt
	v_add_u32_e32 v117, 0x31800, v166
	global_load_dwordx2 v[240:241], v117, s[38:39] nt
	v_add_u32_e32 v117, 0x31800, v167
	global_load_dwordx2 v[242:243], v117, s[38:39] nt
	v_add_u32_e32 v117, 0x33000, v165
	global_load_dwordx2 v[244:245], v117, s[38:39] nt
	v_add_u32_e32 v117, 0x33000, v166
	global_load_dwordx2 v[246:247], v117, s[38:39] nt
	v_add_u32_e32 v117, 0x33000, v167
	global_load_dwordx2 v[248:249], v117, s[38:39] nt
	v_add_u32_e32 v117, 0x34800, v165
	global_load_dwordx2 v[250:251], v117, s[38:39] nt
	v_add_u32_e32 v117, 0x34800, v166
	global_load_dwordx2 v[252:253], v117, s[38:39] nt
	v_add_u32_e32 v117, 0x34800, v167
	global_load_dwordx2 v[254:255], v117, s[38:39] nt
	s_barrier
	v_and_b32_e32 v205, 16, v175
	v_lshrrev_b32_e32 v207, 2, v175
	v_or_b32_e32 v206, v179, v177
	v_and_or_b32 v180, v207, 12, v180
	v_bitop3_b32 v177, v179, v205, v177 bitop3:0x36
	v_lshlrev_b32_e32 v177, 2, v177
	v_mul_lo_u32 v179, v180, s67
	v_add3_u32 v177, 0, v177, v179
	ds_write2st64_b32 v177, v58, v59 offset1:3
	ds_write2st64_b32 v177, v60, v61 offset0:6 offset1:9
	ds_write2st64_b32 v177, v102, v103 offset0:48 offset1:51
	ds_write2st64_b32 v177, v104, v105 offset0:54 offset1:57
	v_add_u32_e32 v58, 16, v206
	v_bitop3_b32 v58, v58, v175, 16 bitop3:0x78
	v_lshlrev_b32_e32 v58, 2, v58
	v_add3_u32 v102, 0, v58, v179
	ds_write2st64_b32 v102, v78, v79 offset1:3
	v_add_u32_e32 v78, 32, v206
	v_bitop3_b32 v78, v78, v175, 16 bitop3:0x78
	v_lshlrev_b32_e32 v78, 2, v78
	v_add3_u32 v103, 0, v78, v179
	ds_write2st64_b32 v102, v80, v81 offset0:6 offset1:9
	ds_write2st64_b32 v102, v86, v87 offset0:48 offset1:51
	ds_write2st64_b32 v102, v88, v89 offset0:54 offset1:57
	ds_write2st64_b32 v103, v62, v63 offset1:3
	ds_write2st64_b32 v103, v64, v65 offset0:6 offset1:9
	ds_write2st64_b32 v103, v70, v71 offset0:48 offset1:51
	ds_write2st64_b32 v103, v72, v73 offset0:54 offset1:57
	v_add_u32_e32 v62, 0x60, v206
	v_bitop3_b32 v62, v62, v175, 16 bitop3:0x78
	v_lshlrev_b32_e32 v62, 2, v62
	v_add3_u32 v104, 0, v62, v179
	v_add_u32_e32 v62, 0x70, v206
	v_bitop3_b32 v62, v62, v175, 16 bitop3:0x78
	v_lshlrev_b32_e32 v62, 2, v62
	s_movk_i32 s2, 0x80
	ds_write2st64_b32 v104, v94, v95 offset1:3
	ds_write2st64_b32 v104, v96, v97 offset0:6 offset1:9
	ds_write2st64_b32 v104, v98, v99 offset0:48 offset1:51
	ds_write2st64_b32 v104, v100, v101 offset0:54 offset1:57
	v_add3_u32 v101, 0, v62, v179
	v_bitop3_b32 v62, v206, v205, s2 bitop3:0x36
	v_lshlrev_b32_e32 v62, 2, v62
	v_add3_u32 v105, 0, v62, v179
	ds_write2st64_b32 v101, v82, v83 offset1:3
	ds_write2st64_b32 v101, v84, v85 offset0:6 offset1:9
	ds_write2st64_b32 v101, v90, v91 offset0:48 offset1:51
	ds_write2st64_b32 v101, v92, v93 offset0:54 offset1:57
	ds_write2st64_b32 v105, v66, v67 offset1:3
	ds_write2st64_b32 v105, v68, v69 offset0:6 offset1:9
	ds_write2st64_b32 v105, v74, v75 offset0:48 offset1:51
	ds_write2st64_b32 v105, v76, v77 offset0:54 offset1:57
	s_waitcnt lgkmcnt(0)
	s_barrier
	ds_read_b128 v[182:185], v156
	ds_read_b128 v[186:189], v157
	ds_read_b128 v[190:193], v158
	ds_read_b128 v[194:197], v159 offset:3072
	ds_read_b128 v[198:201], v160 offset:3072
	ds_read_b128 v[202:205], v161 offset:3072
	ds_read_b128 v[206:209], v156 offset:6144
	ds_read_b128 v[210:213], v157 offset:6144
	ds_read_b128 v[214:217], v158 offset:6144
	ds_read_b128 v[218:221], v159 offset:9216
	ds_read_b128 v[222:225], v160 offset:9216
	ds_read_b128 v[226:229], v161 offset:9216
	s_waitcnt lgkmcnt(0)
	s_barrier
	s_waitcnt vmcnt(12)
	v_cvt_f32_f16_e32 v112, v120
	v_cvt_f32_f16_sdwa v113, v120 dst_sel:DWORD dst_unused:UNUSED_PAD src0_sel:WORD_1
	v_cvt_f32_f16_e32 v114, v121
	v_cvt_f32_f16_sdwa v115, v121 dst_sel:DWORD dst_unused:UNUSED_PAD src0_sel:WORD_1
	ds_write2st64_b32 v177, v14, v15 offset1:3
	v_pk_fma_f32 v[182:183], v[112:113], v[144:145], v[182:183]
	v_pk_fma_f32 v[184:185], v[114:115], v[146:147], v[184:185]
	ds_write2st64_b32 v177, v16, v17 offset0:6 offset1:9
	global_store_dwordx4 v162, v[182:185], s[46:47] nt
	v_cvt_f32_f16_e32 v112, v122
	v_cvt_f32_f16_sdwa v113, v122 dst_sel:DWORD dst_unused:UNUSED_PAD src0_sel:WORD_1
	v_cvt_f32_f16_e32 v114, v123
	v_cvt_f32_f16_sdwa v115, v123 dst_sel:DWORD dst_unused:UNUSED_PAD src0_sel:WORD_1
	ds_write2st64_b32 v177, v38, v39 offset0:48 offset1:51
	v_pk_fma_f32 v[186:187], v[112:113], v[148:149], v[186:187]
	v_pk_fma_f32 v[188:189], v[114:115], v[150:151], v[188:189]
	ds_write2st64_b32 v177, v40, v41 offset0:54 offset1:57
	global_store_dwordx4 v163, v[186:189], s[46:47] nt
	v_cvt_f32_f16_e32 v112, v124
	v_cvt_f32_f16_sdwa v113, v124 dst_sel:DWORD dst_unused:UNUSED_PAD src0_sel:WORD_1
	v_cvt_f32_f16_e32 v114, v125
	v_cvt_f32_f16_sdwa v115, v125 dst_sel:DWORD dst_unused:UNUSED_PAD src0_sel:WORD_1
	ds_write2st64_b32 v102, v6, v7 offset1:3
	v_pk_fma_f32 v[190:191], v[112:113], v[152:153], v[190:191]
	v_pk_fma_f32 v[192:193], v[114:115], v[154:155], v[192:193]
	ds_write2st64_b32 v102, v8, v9 offset0:6 offset1:9
	global_store_dwordx4 v164, v[190:193], s[46:47] nt
	v_cvt_f32_f16_e32 v112, v126
	v_cvt_f32_f16_sdwa v113, v126 dst_sel:DWORD dst_unused:UNUSED_PAD src0_sel:WORD_1
	v_cvt_f32_f16_e32 v114, v127
	v_cvt_f32_f16_sdwa v115, v127 dst_sel:DWORD dst_unused:UNUSED_PAD src0_sel:WORD_1
	v_add_u32_e32 v117, 0x3000, v162
	ds_write2st64_b32 v102, v26, v27 offset0:48 offset1:51
	v_pk_fma_f32 v[194:195], v[112:113], v[144:145], v[194:195]
	v_pk_fma_f32 v[196:197], v[114:115], v[146:147], v[196:197]
	ds_write2st64_b32 v102, v28, v29 offset0:54 offset1:57
	global_store_dwordx4 v117, v[194:197], s[46:47] nt
	v_cvt_f32_f16_e32 v112, v128
	v_cvt_f32_f16_sdwa v113, v128 dst_sel:DWORD dst_unused:UNUSED_PAD src0_sel:WORD_1
	v_cvt_f32_f16_e32 v114, v129
	v_cvt_f32_f16_sdwa v115, v129 dst_sel:DWORD dst_unused:UNUSED_PAD src0_sel:WORD_1
	v_add_u32_e32 v117, 0x3000, v163
	ds_write2st64_b32 v103, v2, v3 offset1:3
	v_pk_fma_f32 v[198:199], v[112:113], v[148:149], v[198:199]
	v_pk_fma_f32 v[200:201], v[114:115], v[150:151], v[200:201]
	ds_write2st64_b32 v103, v4, v5 offset0:6 offset1:9
	global_store_dwordx4 v117, v[198:201], s[46:47] nt
	v_cvt_f32_f16_e32 v112, v130
	v_cvt_f32_f16_sdwa v113, v130 dst_sel:DWORD dst_unused:UNUSED_PAD src0_sel:WORD_1
	v_cvt_f32_f16_e32 v114, v131
	v_cvt_f32_f16_sdwa v115, v131 dst_sel:DWORD dst_unused:UNUSED_PAD src0_sel:WORD_1
	v_add_u32_e32 v117, 0x3000, v164
	ds_write2st64_b32 v103, v18, v19 offset0:48 offset1:51
	v_pk_fma_f32 v[202:203], v[112:113], v[152:153], v[202:203]
	v_pk_fma_f32 v[204:205], v[114:115], v[154:155], v[204:205]
	ds_write2st64_b32 v103, v20, v21 offset0:54 offset1:57
	global_store_dwordx4 v117, v[202:205], s[46:47] nt
	v_cvt_f32_f16_e32 v112, v132
	v_cvt_f32_f16_sdwa v113, v132 dst_sel:DWORD dst_unused:UNUSED_PAD src0_sel:WORD_1
	v_cvt_f32_f16_e32 v114, v133
	v_cvt_f32_f16_sdwa v115, v133 dst_sel:DWORD dst_unused:UNUSED_PAD src0_sel:WORD_1
	v_add_u32_e32 v117, 0x6000, v162
	ds_write2st64_b32 v104, v30, v31 offset1:3
	v_pk_fma_f32 v[206:207], v[112:113], v[144:145], v[206:207]
	v_pk_fma_f32 v[208:209], v[114:115], v[146:147], v[208:209]
	ds_write2st64_b32 v104, v32, v33 offset0:6 offset1:9
	global_store_dwordx4 v117, v[206:209], s[46:47] nt
	v_cvt_f32_f16_e32 v112, v134
	v_cvt_f32_f16_sdwa v113, v134 dst_sel:DWORD dst_unused:UNUSED_PAD src0_sel:WORD_1
	v_cvt_f32_f16_e32 v114, v135
	v_cvt_f32_f16_sdwa v115, v135 dst_sel:DWORD dst_unused:UNUSED_PAD src0_sel:WORD_1
	v_add_u32_e32 v117, 0x6000, v163
	ds_write2st64_b32 v104, v46, v47 offset0:48 offset1:51
	v_pk_fma_f32 v[210:211], v[112:113], v[148:149], v[210:211]
	v_pk_fma_f32 v[212:213], v[114:115], v[150:151], v[212:213]
	ds_write2st64_b32 v104, v48, v49 offset0:54 offset1:57
	global_store_dwordx4 v117, v[210:213], s[46:47] nt
	v_cvt_f32_f16_e32 v112, v136
	v_cvt_f32_f16_sdwa v113, v136 dst_sel:DWORD dst_unused:UNUSED_PAD src0_sel:WORD_1
	v_cvt_f32_f16_e32 v114, v137
	v_cvt_f32_f16_sdwa v115, v137 dst_sel:DWORD dst_unused:UNUSED_PAD src0_sel:WORD_1
	v_add_u32_e32 v117, 0x6000, v164
	ds_write2st64_b32 v101, v22, v23 offset1:3
	v_pk_fma_f32 v[214:215], v[112:113], v[152:153], v[214:215]
	v_pk_fma_f32 v[216:217], v[114:115], v[154:155], v[216:217]
	ds_write2st64_b32 v101, v24, v25 offset0:6 offset1:9
	global_store_dwordx4 v117, v[214:217], s[46:47] nt
	v_cvt_f32_f16_e32 v112, v138
	v_cvt_f32_f16_sdwa v113, v138 dst_sel:DWORD dst_unused:UNUSED_PAD src0_sel:WORD_1
	v_cvt_f32_f16_e32 v114, v139
	v_cvt_f32_f16_sdwa v115, v139 dst_sel:DWORD dst_unused:UNUSED_PAD src0_sel:WORD_1
	v_add_u32_e32 v117, 0x9000, v162
	ds_write2st64_b32 v101, v42, v43 offset0:48 offset1:51
	v_pk_fma_f32 v[218:219], v[112:113], v[144:145], v[218:219]
	v_pk_fma_f32 v[220:221], v[114:115], v[146:147], v[220:221]
	ds_write2st64_b32 v101, v44, v45 offset0:54 offset1:57
	global_store_dwordx4 v117, v[218:221], s[46:47] nt
	v_cvt_f32_f16_e32 v112, v140
	v_cvt_f32_f16_sdwa v113, v140 dst_sel:DWORD dst_unused:UNUSED_PAD src0_sel:WORD_1
	v_cvt_f32_f16_e32 v114, v141
	v_cvt_f32_f16_sdwa v115, v141 dst_sel:DWORD dst_unused:UNUSED_PAD src0_sel:WORD_1
	v_add_u32_e32 v117, 0x9000, v163
	ds_write2st64_b32 v105, v10, v11 offset1:3
	v_pk_fma_f32 v[222:223], v[112:113], v[148:149], v[222:223]
	v_pk_fma_f32 v[224:225], v[114:115], v[150:151], v[224:225]
	ds_write2st64_b32 v105, v12, v13 offset0:6 offset1:9
	global_store_dwordx4 v117, v[222:225], s[46:47] nt
	v_cvt_f32_f16_e32 v112, v142
	v_cvt_f32_f16_sdwa v113, v142 dst_sel:DWORD dst_unused:UNUSED_PAD src0_sel:WORD_1
	v_cvt_f32_f16_e32 v114, v143
	v_cvt_f32_f16_sdwa v115, v143 dst_sel:DWORD dst_unused:UNUSED_PAD src0_sel:WORD_1
	v_add_u32_e32 v117, 0x9000, v164
	ds_write2st64_b32 v105, v34, v35 offset0:48 offset1:51
	v_pk_fma_f32 v[226:227], v[112:113], v[152:153], v[226:227]
	v_pk_fma_f32 v[228:229], v[114:115], v[154:155], v[228:229]
	ds_write2st64_b32 v105, v36, v37 offset0:54 offset1:57
	global_store_dwordx4 v117, v[226:229], s[46:47] nt
	s_waitcnt lgkmcnt(0)
	s_barrier
	s_and_saveexec_b64 s[100:101], s[34:35]
	s_cbranch_execz .Lpf_skip_g2
	v_readfirstlane_b32 s10, v173
	s_lshl_b32 s10, s10, 7
	s_add_u32 s10, s64, s10
	s_addc_u32 s11, s65, 0
	global_atomic_add v231, v109, v1, s[10:11] sc0
